# speedup vs baseline: 1.0089x; 1.0009x over previous
_Z11attn_kernelPKDF16_S0_S0_PDF16_P15HIP_vector_typeIfLj2EE:
	s_mov_b32 s28, s2
	s_load_dwordx4 s[32:35], s[0:1], 0x8
	v_readfirstlane_b32 s3, v0
	s_ashr_i32 s12, s2, 5
	s_lshr_b32 s21, s3, 6
	s_and_b32 s3, s2, 7
	s_and_b32 s12, s12, -8
	s_load_dwordx8 s[4:11], s[0:1], 0x0
	s_or_b32 s12, s12, s3
	s_bfe_u32 s20, s2, 0x10003
	s_lshl_b32 s2, s2, 3
	s_and_b32 s2, s2, 0x780
	s_lshl_b32 s3, s21, 5
	s_ashr_i32 s13, s12, 31
	s_add_i32 s2, s3, s2
	s_lshl_b64 s[16:17], s[12:13], 11
	s_lshl_b32 s3, s20, 10
	s_or_b32 s14, s16, s3
	s_mov_b32 s15, s17
	s_lshl_b64 s[18:19], s[14:15], 7
	s_lshl_b64 s[14:15], s[12:13], 18
	s_waitcnt lgkmcnt(0)
	s_add_u32 s3, s8, s14
	s_addc_u32 s22, s9, s15
	s_add_u32 s16, s16, s2
	v_and_b32_e32 v98, 31, v0
	s_addc_u32 s17, s17, 0
	v_or_b32_e32 v2, s16, v98
	v_mov_b32_e32 v3, s17
	v_bfe_u32 v54, v0, 5, 1
	v_lshlrev_b64 v[2:3], 7, v[2:3]
	v_mov_b32_e32 v51, 0
	v_lshl_add_u64 v[2:3], s[4:5], 0, v[2:3]
	v_lshlrev_b32_e32 v50, 4, v54
	v_lshl_add_u64 v[2:3], v[2:3], 0, v[50:51]
	s_add_u32 s18, s6, s18
	v_bfe_u32 v1, v0, 3, 3
	global_load_dwordx4 v[94:97], v[2:3], off nt
	global_load_dwordx4 v[90:93], v[2:3], off offset:32 nt
	global_load_dwordx4 v[86:89], v[2:3], off offset:64 nt
	global_load_dwordx4 v[82:85], v[2:3], off offset:96 nt
	s_addc_u32 s19, s7, s19
	s_lshl_b32 s24, s20, 11
	v_lshl_or_b32 v2, s21, 4, v1
	v_and_b32_e32 v99, 63, v0
	s_add_u32 s4, s3, s24
	v_or_b32_e32 v3, 8, v2
	v_lshlrev_b32_e32 v4, 4, v0
	s_movk_i32 s3, 0x70
	v_bitop3_b32 v53, v99, s3, v4 bitop3:0x48
	v_lshrrev_b32_e32 v4, 1, v3
	v_xor_b32_e32 v4, v4, v0
	s_addc_u32 s5, s22, 0
	v_lshlrev_b32_e32 v4, 4, v4
	s_lshl_b32 s22, s21, 11
	v_and_b32_e32 v52, 0x70, v4
	v_lshl_or_b32 v55, v2, 7, v53
	s_mov_b32 m0, s22
	v_lshl_or_b32 v64, v3, 7, v52
	global_load_lds_dwordx4 v55, s[18:19]
	s_or_b32 m0, s22, 0x400
	v_lshl_or_b32 v50, v2, 12, v53
	global_load_lds_dwordx4 v64, s[18:19]
	s_add_i32 m0, s22, 0x2000
	v_lshl_or_b32 v2, v3, 12, v52
	global_load_lds_dwordx4 v50, s[4:5]
	s_add_i32 m0, s22, 0x2400
	v_mov_b32_e32 v3, v51
	global_load_lds_dwordx4 v2, s[4:5]
	s_add_i32 m0, s22, 0x4000
	v_lshl_add_u64 v[60:61], s[4:5], 0, v[50:51]
	v_lshl_add_u64 v[62:63], s[4:5], 0, v[2:3]
	s_add_u32 s4, s18, 0x2000
	s_addc_u32 s5, s19, 0
	s_add_i32 m0, s22, 0x4400
	s_load_dwordx2 s[0:1], s[0:1], 0x20
	s_mov_b64 s[4:5], 0x80
	v_lshl_add_u64 v[2:3], v[60:61], 0, s[4:5]
	s_add_i32 m0, s22, 0x6000
	v_lshrrev_b32_e32 v4, 1, v0
	v_lshl_add_u64 v[2:3], v[62:63], 0, s[4:5]
	s_add_i32 m0, s22, 0x6400
	v_and_b32_e32 v5, 4, v4
	v_lshlrev_b32_e32 v3, 1, v0
	v_and_b32_e32 v2, 19, v0
	v_and_b32_e32 v3, 8, v3
	v_or3_b32 v2, v3, v2, v5
	s_waitcnt vmcnt(0)
	v_lshlrev_b32_e32 v115, 7, v2
	v_lshrrev_b32_e32 v3, 1, v2
	v_bfe_u32 v46, v2, 1, 3
	v_bitop3_b32 v2, v54, v4, 7 bitop3:0x78
	s_mov_b32 s3, 0
	v_lshlrev_b32_e32 v108, 3, v54
	s_mov_b32 s23, 1
	s_mov_b64 s[16:17], 0x2000
	v_lshlrev_b32_e32 v109, 7, v98
	v_lshlrev_b32_e32 v110, 4, v2
	s_movk_i32 s25, 0x400
	v_bfe_u32 v50, v0, 1, 3
	s_barrier
	s_and_b32 s29, s28, 7
	s_lshr_b32 s40, s28, 3
	s_lshr_b32 s41, s40, 5
	s_lshl_b32 s41, s41, 3
	s_or_b32 s29, s41, s29
	s_and_b32 s40, s40, 1
	s_lshl_b32 s29, s29, 18
	s_lshl_b32 s41, s40, 17
	s_lshl_b32 s42, s40, 11
	s_add_i32 s41, s41, s29
	s_add_i32 s41, s41, 0x6000
	s_add_i32 s42, s42, s29
	s_add_i32 s42, s42, 0x180
	v_and_b32_e32 v145, 63, v0
	v_lshrrev_b32_e32 v146, 3, v145
	v_lshl_add_u32 v146, s21, 4, v146
	v_and_b32_e32 v145, 7, v145
	v_bfe_u32 v147, v146, 1, 3
	v_xor_b32_e32 v148, v145, v147
	v_xor_b32_e32 v147, 4, v148
	v_lshlrev_b32_e32 v148, 4, v148
	v_lshlrev_b32_e32 v147, 4, v147
	v_lshl_add_u32 v145, v146, 7, v148
	v_lshl_add_u32 v149, v146, 7, v147
	v_lshl_add_u32 v148, v146, 12, v148
	v_lshl_add_u32 v147, v146, 12, v147
	v_add_u32_e32 v147, 0x7c00, v147
	s_waitcnt lgkmcnt(0)
	s_add_u32 s36, s32, s41
	s_addc_u32 s37, s33, 0
	s_add_u32 s38, s34, s42
	s_addc_u32 s39, s35, 0
	s_sub_u32 s40, s36, 0x4000
	s_subb_u32 s41, s37, 0
	s_sub_u32 s42, s38, 0x100
	s_subb_u32 s43, s39, 0
	s_add_i32 m0, s22, 0x4000
	s_nop 0
	global_load_lds_dwordx4 v145, s[40:41]
	global_load_lds_dwordx4 v149, s[40:41] offset:1024
	s_add_i32 m0, s22, 0x6000
	s_nop 0
	global_load_lds_dwordx4 v148, s[42:43]
	global_load_lds_dwordx4 v147, s[42:43] offset:1024
	v_bitop3_b32 v2, v54, v3, 7 bitop3:0x78
	v_lshlrev_b32_e32 v116, 4, v2
	v_bitop3_b32 v6, v54, v46, 2 bitop3:0x36
	v_lshlrev_b32_e32 v117, 4, v6
	v_bitop3_b32 v42, v54, v46, 4 bitop3:0x36
	v_bitop3_b32 v46, v54, v46, 6 bitop3:0x36
	v_lshlrev_b32_e32 v118, 4, v42
	v_lshlrev_b32_e32 v119, 4, v46
	v_bitop3_b32 v10, v54, v50, 2 bitop3:0x36
	v_lshlrev_b32_e32 v112, 4, v10
	v_bitop3_b32 v55, v54, v50, 4 bitop3:0x36
	v_bitop3_b32 v50, v54, v50, 6 bitop3:0x36
	v_lshlrev_b32_e32 v111, 4, v55
	v_lshlrev_b32_e32 v113, 4, v50
	v_mov_b32_e32 v2, 0
	v_mov_b32_e32 v3, 0
	v_mov_b32_e32 v4, 0
	v_mov_b32_e32 v5, 0
	v_mov_b32_e32 v6, 0
	v_mov_b32_e32 v7, 0
	v_mov_b32_e32 v8, 0
	v_mov_b32_e32 v9, 0
	v_mov_b32_e32 v10, 0
	v_mov_b32_e32 v11, 0
	v_mov_b32_e32 v12, 0
	v_mov_b32_e32 v13, 0
	v_mov_b32_e32 v14, 0
	v_mov_b32_e32 v15, 0
	v_mov_b32_e32 v16, 0
	v_mov_b32_e32 v17, 0
	v_mov_b32_e32 v18, 0
	v_mov_b32_e32 v19, 0
	v_mov_b32_e32 v20, 0
	v_mov_b32_e32 v21, 0
	v_mov_b32_e32 v22, 0
	v_mov_b32_e32 v23, 0
	v_mov_b32_e32 v24, 0
	v_mov_b32_e32 v25, 0
	v_mov_b32_e32 v26, 0
	v_mov_b32_e32 v27, 0
	v_mov_b32_e32 v28, 0
	v_mov_b32_e32 v29, 0
	v_mov_b32_e32 v30, 0
	v_mov_b32_e32 v31, 0
	v_mov_b32_e32 v32, 0
	v_mov_b32_e32 v33, 0
	v_mov_b32_e32 v34, 0
	v_mov_b32_e32 v35, 0
	v_mov_b32_e32 v36, 0
	v_mov_b32_e32 v37, 0
	v_mov_b32_e32 v38, 0
	v_mov_b32_e32 v39, 0
	v_mov_b32_e32 v40, 0
	v_mov_b32_e32 v41, 0
	v_mov_b32_e32 v42, 0
	v_mov_b32_e32 v43, 0
	v_mov_b32_e32 v44, 0
	v_mov_b32_e32 v45, 0
	v_mov_b32_e32 v46, 0
	v_mov_b32_e32 v47, 0
	v_mov_b32_e32 v48, 0
	v_mov_b32_e32 v49, 0
	v_mov_b32_e32 v114, 0
	s_mov_b32 s23, 0
	s_mov_b32 s9, 0
	s_mov_b32 s8, 0x46000000
	s_sub_u32 s36, s36, 0x2000
	s_subb_u32 s37, s37, 0
	s_sub_u32 s38, s38, 0x80
	s_subb_u32 s39, s39, 0
	s_mov_b32 s44, 0xff800000
	s_mov_b32 s45, 0x3c800000
.LBB3_1:
	s_waitcnt vmcnt(4)
	s_lshl_b32 s18, s23, 14
	s_barrier
	v_or_b32_e32 v144, s18, v115
	v_add_u32_e32 v154, v144, v116
	v_add_u32_e32 v155, v144, v117
	v_add_u32_e32 v156, v144, v118
	v_add_u32_e32 v157, v144, v119
	ds_read_b128 v[50:53], v154
	ds_read_b128 v[120:123], v154 offset:4096
	ds_read_b128 v[124:127], v155
	ds_read_b128 v[128:131], v155 offset:4096
	ds_read_b128 v[132:135], v156
	ds_read_b128 v[136:139], v156 offset:4096
	ds_read_b128 v[140:143], v157
	ds_read_b128 v[150:153], v157 offset:4096
	s_add_i32 s6, s18, 0xffffc000
	s_cmp_lg_u32 s23, 0
	s_cselect_b32 s6, s6, 0x8000
	s_add_i32 s6, s22, s6
	s_waitcnt lgkmcnt(4)
	s_setprio 1
	v_mfma_f32_32x32x16_f16 v[66:81], v[50:53], v[94:97], v[34:49]
	s_mov_b32 m0, s6
	s_add_i32 s7, s6, 0x2000
	v_mfma_f32_32x32x16_f16 v[50:65], v[120:123], v[94:97], v[34:49]
	global_load_lds_dwordx4 v145, s[36:37]
	v_mfma_f32_32x32x16_f16 v[66:81], v[124:127], v[90:93], v[66:81]
	global_load_lds_dwordx4 v149, s[36:37] offset:1024
	v_mfma_f32_32x32x16_f16 v[50:65], v[128:131], v[90:93], v[50:65]
	s_mov_b32 m0, s7
	s_waitcnt lgkmcnt(0)
	v_mfma_f32_32x32x16_f16 v[66:81], v[132:135], v[86:89], v[66:81]
	global_load_lds_dwordx4 v148, s[38:39]
	v_mfma_f32_32x32x16_f16 v[50:65], v[136:139], v[86:89], v[50:65]
	global_load_lds_dwordx4 v147, s[38:39] offset:1024
	v_mfma_f32_32x32x16_f16 v[66:81], v[140:143], v[82:85], v[66:81]
	v_mfma_f32_32x32x16_f16 v[50:65], v[150:153], v[82:85], v[50:65]
	s_setprio 0
	s_add_u32 s36, s36, 0x2000
	s_addc_u32 s37, s37, 0
	s_add_u32 s38, s38, 0x80
	s_addc_u32 s39, s39, 0
	s_nop 1
